# fp8 GEMM units (in-proj fp8, GEMM1, GEMM2): first-iteration vmcnt(8) waits relaxed to vmcnt(8+S) for non-first units so the previous epilogue's S stores stay in flight; on top of NA mask rewrite
# speedup vs baseline: 1.0486x; 1.0065x over previous
.LBB0_387:
	s_ashr_i32 s35, s34, 31
	ds_read_b128 v[18:21], v180
	ds_read_b128 v[22:25], v181
	ds_read_b128 v[26:29], v182
	ds_read_b128 v[30:33], v183
	ds_read_b128 v[2:5], v184
	ds_read_b128 v[6:9], v185
	ds_read_b128 v[10:13], v186
	ds_read_b128 v[14:17], v187
	s_lshl_b64 s[26:27], s[34:35], 18
	s_add_u32 s38, s53, s26
	s_addc_u32 s39, s54, s27
	s_and_b64 s[26:27], s[42:43], exec
	s_cselect_b32 s1, s39, s47
	s_cselect_b32 s5, s38, s46
	s_ashr_i32 s37, s36, 31
	s_lshl_b64 s[26:27], s[36:37], 18
	s_add_u32 s40, s55, s26
	s_addc_u32 s41, s56, s27
	s_and_b64 s[26:27], s[42:43], exec
	s_cselect_b32 s23, s41, s45
	s_cselect_b32 s26, s40, s44
	s_add_u32 s48, s46, 0x20080
	s_addc_u32 s49, s47, 0
	s_add_i32 s27, s57, 0xc000
	v_lshl_add_u64 v[224:225], s[48:49], 0, v[162:163]
	s_mov_b32 m0, s27
	s_add_i32 s35, s57, 0xe000
	ds_read_b128 v[172:175], v196
	ds_read_b128 v[176:179], v196 offset:1024
	ds_read_b128 v[198:201], v196 offset:2048
	ds_read_b128 v[202:205], v196 offset:3072
	ds_read_b128 v[206:209], v196 offset:4096
	ds_read_b128 v[210:213], v196 offset:5120
	ds_read_b128 v[216:219], v196 offset:6144
	ds_read_b128 v[220:223], v196 offset:7168
	global_load_lds_dwordx4 v[224:225], off
	v_lshl_add_u64 v[224:225], s[48:49], 0, v[164:165]
	s_mov_b32 m0, s35
	s_nop 0
	global_load_lds_dwordx4 v[224:225], off
	s_cmp_eq_u32 s50, 1
	s_cbranch_scc1 .Lrw_first_ip8_0
	s_waitcnt vmcnt(24)
	s_branch .Lrw_done_ip8_0
.Lrw_first_ip8_0:
	s_waitcnt vmcnt(8)
.Lrw_done_ip8_0:
	s_waitcnt lgkmcnt(0)
	s_barrier
	s_setprio 1
	s_waitcnt lgkmcnt(0)
	v_mfma_scale_f32_16x16x128_f8f6f4 v[158:161], v[18:25], v[172:179], 0, v234, v235 op_sel_hi:[0,0,0]
	v_mfma_scale_f32_16x16x128_f8f6f4 v[154:157], v[26:33], v[172:179], 0, v234, v235 op_sel_hi:[0,0,0]
	v_mfma_scale_f32_16x16x128_f8f6f4 v[150:153], v[18:25], v[198:205], 0, v234, v235 op_sel_hi:[0,0,0]
	v_mfma_scale_f32_16x16x128_f8f6f4 v[146:149], v[26:33], v[198:205], 0, v234, v235 op_sel_hi:[0,0,0]
	v_mfma_scale_f32_16x16x128_f8f6f4 v[142:145], v[18:25], v[206:213], 0, v234, v235 op_sel_hi:[0,0,0]
	v_mfma_scale_f32_16x16x128_f8f6f4 v[138:141], v[26:33], v[206:213], 0, v234, v235 op_sel_hi:[0,0,0]
	v_mfma_scale_f32_16x16x128_f8f6f4 v[134:137], v[18:25], v[216:223], 0, v234, v235 op_sel_hi:[0,0,0]
	v_mfma_scale_f32_16x16x128_f8f6f4 v[130:133], v[26:33], v[216:223], 0, v234, v235 op_sel_hi:[0,0,0]
	s_setprio 0
	s_setprio 1
	v_mfma_scale_f32_16x16x128_f8f6f4 v[126:129], v[2:9], v[172:179], 0, v234, v235 op_sel_hi:[0,0,0]
	v_mfma_scale_f32_16x16x128_f8f6f4 v[122:125], v[10:17], v[172:179], 0, v234, v235 op_sel_hi:[0,0,0]
	v_mfma_scale_f32_16x16x128_f8f6f4 v[118:121], v[2:9], v[198:205], 0, v234, v235 op_sel_hi:[0,0,0]
	v_mfma_scale_f32_16x16x128_f8f6f4 v[114:117], v[10:17], v[198:205], 0, v234, v235 op_sel_hi:[0,0,0]
	v_mfma_scale_f32_16x16x128_f8f6f4 v[110:113], v[2:9], v[206:213], 0, v234, v235 op_sel_hi:[0,0,0]
	v_mfma_scale_f32_16x16x128_f8f6f4 v[106:109], v[10:17], v[206:213], 0, v234, v235 op_sel_hi:[0,0,0]
	v_mfma_scale_f32_16x16x128_f8f6f4 v[102:105], v[2:9], v[216:223], 0, v234, v235 op_sel_hi:[0,0,0]
	v_mfma_scale_f32_16x16x128_f8f6f4 v[98:101], v[10:17], v[216:223], 0, v234, v235 op_sel_hi:[0,0,0]
	s_setprio 0
	s_barrier
	v_lshl_add_u64 v[172:173], s[44:45], 0, v[0:1]
	s_mov_b64 s[74:75], 0x100
	s_mov_b32 m0, s58
	v_lshl_add_u64 v[174:175], v[172:173], 0, s[74:75]
	ds_read_b128 v[198:201], v196 offset:16384
	ds_read_b128 v[202:205], v196 offset:17408
	ds_read_b128 v[206:209], v196 offset:18432
	ds_read_b128 v[210:213], v196 offset:19456
	ds_read_b128 v[216:219], v196 offset:20480
	ds_read_b128 v[220:223], v196 offset:21504
	ds_read_b128 v[224:227], v196 offset:22528
	ds_read_b128 v[228:231], v196 offset:23552
	global_load_lds_dwordx4 v[174:175], off
	v_lshl_add_u64 v[174:175], s[44:45], 0, v[166:167]
	s_add_u32 s48, s44, 0x20100
	v_lshl_add_u64 v[176:177], v[174:175], 0, s[74:75]
	s_mov_b32 m0, s59
	s_addc_u32 s49, s45, 0
	global_load_lds_dwordx4 v[176:177], off
	v_lshl_add_u64 v[176:177], s[48:49], 0, v[0:1]
	s_mov_b32 m0, s60
	s_nop 0
	global_load_lds_dwordx4 v[176:177], off
	v_lshl_add_u64 v[176:177], s[48:49], 0, v[166:167]
	s_mov_b32 m0, s61
	s_nop 0
	global_load_lds_dwordx4 v[176:177], off
	v_lshl_add_u64 v[176:177], s[46:47], 0, v[162:163]
	v_lshl_add_u64 v[178:179], v[176:177], 0, s[74:75]
	s_mov_b32 m0, s57
	s_nop 0
	global_load_lds_dwordx4 v[178:179], off
	v_lshl_add_u64 v[178:179], s[46:47], 0, v[164:165]
	v_lshl_add_u64 v[232:233], v[178:179], 0, s[74:75]
	s_mov_b32 m0, s62
	s_nop 0
	global_load_lds_dwordx4 v[232:233], off
	s_cmp_eq_u32 s50, 1
	s_cbranch_scc1 .Lrw_first_ip8_1
	s_waitcnt vmcnt(24)
	s_branch .Lrw_done_ip8_1

.Lrw_done_ip8_1:
	s_waitcnt lgkmcnt(0)
	s_barrier
	s_setprio 1
	s_waitcnt lgkmcnt(0)
	v_mfma_scale_f32_16x16x128_f8f6f4 v[94:97], v[18:25], v[198:205], 0, v234, v235 op_sel_hi:[0,0,0]
	v_mfma_scale_f32_16x16x128_f8f6f4 v[90:93], v[26:33], v[198:205], 0, v234, v235 op_sel_hi:[0,0,0]
	v_mfma_scale_f32_16x16x128_f8f6f4 v[86:89], v[18:25], v[206:213], 0, v234, v235 op_sel_hi:[0,0,0]
	v_mfma_scale_f32_16x16x128_f8f6f4 v[82:85], v[26:33], v[206:213], 0, v234, v235 op_sel_hi:[0,0,0]
	v_mfma_scale_f32_16x16x128_f8f6f4 v[78:81], v[18:25], v[216:223], 0, v234, v235 op_sel_hi:[0,0,0]
	v_mfma_scale_f32_16x16x128_f8f6f4 v[74:77], v[26:33], v[216:223], 0, v234, v235 op_sel_hi:[0,0,0]
	v_mfma_scale_f32_16x16x128_f8f6f4 v[70:73], v[18:25], v[224:231], 0, v234, v235 op_sel_hi:[0,0,0]
	v_mfma_scale_f32_16x16x128_f8f6f4 v[66:69], v[26:33], v[224:231], 0, v234, v235 op_sel_hi:[0,0,0]
	s_setprio 0
	s_setprio 1
	v_mfma_scale_f32_16x16x128_f8f6f4 v[62:65], v[2:9], v[198:205], 0, v234, v235 op_sel_hi:[0,0,0]
	v_mfma_scale_f32_16x16x128_f8f6f4 v[58:61], v[10:17], v[198:205], 0, v234, v235 op_sel_hi:[0,0,0]
	v_mfma_scale_f32_16x16x128_f8f6f4 v[54:57], v[2:9], v[206:213], 0, v234, v235 op_sel_hi:[0,0,0]
	v_mfma_scale_f32_16x16x128_f8f6f4 v[50:53], v[10:17], v[206:213], 0, v234, v235 op_sel_hi:[0,0,0]
	v_mfma_scale_f32_16x16x128_f8f6f4 v[46:49], v[2:9], v[216:223], 0, v234, v235 op_sel_hi:[0,0,0]
	v_mfma_scale_f32_16x16x128_f8f6f4 v[42:45], v[10:17], v[216:223], 0, v234, v235 op_sel_hi:[0,0,0]
	v_mfma_scale_f32_16x16x128_f8f6f4 v[38:41], v[2:9], v[224:231], 0, v234, v235 op_sel_hi:[0,0,0]
	v_mfma_scale_f32_16x16x128_f8f6f4 v[34:37], v[10:17], v[224:231], 0, v234, v235 op_sel_hi:[0,0,0]
	s_setprio 0
	s_barrier
	ds_read_b128 v[18:21], v188
	ds_read_b128 v[22:25], v189
	ds_read_b128 v[26:29], v190
	ds_read_b128 v[30:33], v191
	ds_read_b128 v[2:5], v192
	ds_read_b128 v[6:9], v193
	ds_read_b128 v[10:13], v194
	ds_read_b128 v[14:17], v195
	s_add_u32 s48, s46, 0x20100
	s_addc_u32 s49, s47, 0
	s_mov_b32 m0, s63
	v_lshl_add_u64 v[232:233], s[48:49], 0, v[162:163]
	ds_read_b128 v[198:201], v196 offset:32768
	ds_read_b128 v[202:205], v196 offset:33792
	ds_read_b128 v[206:209], v196 offset:34816
	ds_read_b128 v[210:213], v196 offset:35840
	ds_read_b128 v[216:219], v196 offset:36864
	ds_read_b128 v[220:223], v196 offset:37888
	ds_read_b128 v[224:227], v196 offset:38912
	ds_read_b128 v[228:231], v196 offset:39936
	global_load_lds_dwordx4 v[232:233], off
	v_lshl_add_u64 v[232:233], s[48:49], 0, v[164:165]
	s_mov_b32 m0, s64
	s_nop 0
	global_load_lds_dwordx4 v[232:233], off
	s_waitcnt vmcnt(8)
	s_waitcnt lgkmcnt(0)
	s_barrier
	s_setprio 1
	s_waitcnt lgkmcnt(0)
	v_mfma_scale_f32_16x16x128_f8f6f4 v[158:161], v[18:25], v[198:205], v[158:161], v234, v235 op_sel_hi:[0,0,0]
	v_mfma_scale_f32_16x16x128_f8f6f4 v[154:157], v[26:33], v[198:205], v[154:157], v234, v235 op_sel_hi:[0,0,0]
	v_mfma_scale_f32_16x16x128_f8f6f4 v[150:153], v[18:25], v[206:213], v[150:153], v234, v235 op_sel_hi:[0,0,0]
	v_mfma_scale_f32_16x16x128_f8f6f4 v[146:149], v[26:33], v[206:213], v[146:149], v234, v235 op_sel_hi:[0,0,0]
	v_mfma_scale_f32_16x16x128_f8f6f4 v[142:145], v[18:25], v[216:223], v[142:145], v234, v235 op_sel_hi:[0,0,0]
	v_mfma_scale_f32_16x16x128_f8f6f4 v[138:141], v[26:33], v[216:223], v[138:141], v234, v235 op_sel_hi:[0,0,0]
	v_mfma_scale_f32_16x16x128_f8f6f4 v[134:137], v[18:25], v[224:231], v[134:137], v234, v235 op_sel_hi:[0,0,0]
	v_mfma_scale_f32_16x16x128_f8f6f4 v[130:133], v[26:33], v[224:231], v[130:133], v234, v235 op_sel_hi:[0,0,0]
	s_setprio 0
	s_setprio 1
	v_mfma_scale_f32_16x16x128_f8f6f4 v[126:129], v[2:9], v[198:205], v[126:129], v234, v235 op_sel_hi:[0,0,0]
	v_mfma_scale_f32_16x16x128_f8f6f4 v[122:125], v[10:17], v[198:205], v[122:125], v234, v235 op_sel_hi:[0,0,0]
	v_mfma_scale_f32_16x16x128_f8f6f4 v[118:121], v[2:9], v[206:213], v[118:121], v234, v235 op_sel_hi:[0,0,0]
	v_mfma_scale_f32_16x16x128_f8f6f4 v[114:117], v[10:17], v[206:213], v[114:117], v234, v235 op_sel_hi:[0,0,0]
	v_mfma_scale_f32_16x16x128_f8f6f4 v[110:113], v[2:9], v[216:223], v[110:113], v234, v235 op_sel_hi:[0,0,0]
	v_mfma_scale_f32_16x16x128_f8f6f4 v[106:109], v[10:17], v[216:223], v[106:109], v234, v235 op_sel_hi:[0,0,0]
	v_mfma_scale_f32_16x16x128_f8f6f4 v[102:105], v[2:9], v[224:231], v[102:105], v234, v235 op_sel_hi:[0,0,0]
	v_mfma_scale_f32_16x16x128_f8f6f4 v[98:101], v[10:17], v[224:231], v[98:101], v234, v235 op_sel_hi:[0,0,0]
	s_setprio 0
	s_barrier
	s_mov_b64 s[74:75], 0x180
	s_mov_b32 m0, s7
	v_lshl_add_u64 v[172:173], v[172:173], 0, s[74:75]
	s_add_u32 s48, s44, 0x20180
	ds_read_b128 v[198:201], v196 offset:49152
	ds_read_b128 v[202:205], v196 offset:50176
	ds_read_b128 v[206:209], v196 offset:51200
	ds_read_b128 v[210:213], v196 offset:52224
	ds_read_b128 v[216:219], v196 offset:53248
	ds_read_b128 v[220:223], v196 offset:54272
	ds_read_b128 v[224:227], v196 offset:55296
	ds_read_b128 v[228:231], v196 offset:56320
	global_load_lds_dwordx4 v[172:173], off
	v_lshl_add_u64 v[172:173], v[174:175], 0, s[74:75]
	s_mov_b32 m0, s65
	s_addc_u32 s49, s45, 0
	global_load_lds_dwordx4 v[172:173], off
	v_lshl_add_u64 v[172:173], s[48:49], 0, v[0:1]
	s_mov_b32 m0, s13
	s_nop 0
	global_load_lds_dwordx4 v[172:173], off
	v_lshl_add_u64 v[172:173], s[48:49], 0, v[166:167]
	s_mov_b32 m0, s51
	s_nop 0
	global_load_lds_dwordx4 v[172:173], off
	v_lshl_add_u64 v[172:173], v[176:177], 0, s[74:75]
	s_mov_b32 m0, s68
	s_nop 0
	global_load_lds_dwordx4 v[172:173], off
	v_lshl_add_u64 v[172:173], v[178:179], 0, s[74:75]
	s_mov_b32 m0, s52
	s_nop 0
	global_load_lds_dwordx4 v[172:173], off
	s_waitcnt vmcnt(8)
	s_waitcnt lgkmcnt(0)
	s_barrier
	s_setprio 1
	s_waitcnt lgkmcnt(0)
	v_mfma_scale_f32_16x16x128_f8f6f4 v[94:97], v[18:25], v[198:205], v[94:97], v234, v235 op_sel_hi:[0,0,0]
	v_mfma_scale_f32_16x16x128_f8f6f4 v[90:93], v[26:33], v[198:205], v[90:93], v234, v235 op_sel_hi:[0,0,0]
	v_mfma_scale_f32_16x16x128_f8f6f4 v[86:89], v[18:25], v[206:213], v[86:89], v234, v235 op_sel_hi:[0,0,0]
	v_mfma_scale_f32_16x16x128_f8f6f4 v[82:85], v[26:33], v[206:213], v[82:85], v234, v235 op_sel_hi:[0,0,0]
	v_mfma_scale_f32_16x16x128_f8f6f4 v[78:81], v[18:25], v[216:223], v[78:81], v234, v235 op_sel_hi:[0,0,0]
	v_mfma_scale_f32_16x16x128_f8f6f4 v[74:77], v[26:33], v[216:223], v[74:77], v234, v235 op_sel_hi:[0,0,0]
	v_mfma_scale_f32_16x16x128_f8f6f4 v[70:73], v[18:25], v[224:231], v[70:73], v234, v235 op_sel_hi:[0,0,0]
	v_mfma_scale_f32_16x16x128_f8f6f4 v[66:69], v[26:33], v[224:231], v[66:69], v234, v235 op_sel_hi:[0,0,0]
	s_setprio 0
	s_setprio 1
	v_mfma_scale_f32_16x16x128_f8f6f4 v[62:65], v[2:9], v[198:205], v[62:65], v234, v235 op_sel_hi:[0,0,0]
	v_mfma_scale_f32_16x16x128_f8f6f4 v[58:61], v[10:17], v[198:205], v[58:61], v234, v235 op_sel_hi:[0,0,0]
	v_mfma_scale_f32_16x16x128_f8f6f4 v[54:57], v[2:9], v[206:213], v[54:57], v234, v235 op_sel_hi:[0,0,0]
	v_mfma_scale_f32_16x16x128_f8f6f4 v[50:53], v[10:17], v[206:213], v[50:53], v234, v235 op_sel_hi:[0,0,0]
	v_mfma_scale_f32_16x16x128_f8f6f4 v[46:49], v[2:9], v[216:223], v[46:49], v234, v235 op_sel_hi:[0,0,0]
	v_mfma_scale_f32_16x16x128_f8f6f4 v[42:45], v[10:17], v[216:223], v[42:45], v234, v235 op_sel_hi:[0,0,0]
	v_mfma_scale_f32_16x16x128_f8f6f4 v[38:41], v[2:9], v[224:231], v[38:41], v234, v235 op_sel_hi:[0,0,0]
	v_mfma_scale_f32_16x16x128_f8f6f4 v[34:37], v[10:17], v[224:231], v[34:37], v234, v235 op_sel_hi:[0,0,0]
	s_setprio 0
	s_barrier
	s_add_u32 s46, s46, 0x20180
	s_addc_u32 s47, s47, 0
	s_add_u32 s37, s44, 0x200
	s_addc_u32 s74, s45, 0
	s_mov_b32 s75, 0

.LBB0_2001:
	ds_read_b128 v[6:9], v176
	ds_read_b128 v[2:5], v177
	ds_read_b128 v[14:17], v178
	ds_read_b128 v[10:13], v179
	ds_read_b128 v[22:25], v180
	ds_read_b128 v[18:21], v181
	ds_read_b128 v[30:33], v182
	ds_read_b128 v[26:29], v183
	s_lshl_b32 s26, s31, 10
	s_and_b32 s26, s26, 0x400
	s_add_i32 s26, s26, 0
	s_add_i32 s26, s26, 0x23000
	v_lshlrev_b32_e32 v0, 10, v196
	s_add_i32 s27, s65, 0xc000
	v_and_or_b32 v166, v0, s82, v174
	v_bfe_u32 v0, v196, 16, 16
	s_mov_b32 m0, s27
	s_add_i32 s41, s65, 0xe000
	ds_read_b128 v[198:201], v192
	ds_read_b128 v[202:205], v192 offset:1024
	ds_read_b128 v[206:209], v192 offset:2048
	ds_read_b128 v[210:213], v192 offset:3072
	ds_read_b128 v[216:219], v192 offset:4096
	ds_read_b128 v[220:223], v192 offset:5120
	ds_read_b128 v[224:227], v192 offset:6144
	ds_read_b128 v[228:231], v192 offset:7168
	v_lshl_add_u32 v168, v0, 10, v175
	global_load_lds_dwordx4 v166, s[28:29]
	s_mov_b32 m0, s41
	v_mov_b32_e32 v167, v1
	global_load_lds_dwordx4 v168, s[28:29]
	s_cmp_eq_u32 s23, 0
	s_cbranch_scc1 .Lrw_first_g1_0
	s_waitcnt vmcnt(12)
	s_branch .Lrw_done_g1_0

.Lrw_done_g1_0:
	s_waitcnt lgkmcnt(0)
	v_mov_b32_e32 v169, v1
	s_barrier
	s_setprio 1
	s_waitcnt lgkmcnt(0)
	v_mfma_scale_f32_16x16x128_f8f6f4 v[150:153], v[26:33], v[198:205], 0, v234, v235 op_sel_hi:[0,0,0]
	v_mfma_scale_f32_16x16x128_f8f6f4 v[146:149], v[18:25], v[198:205], 0, v234, v235 op_sel_hi:[0,0,0]
	v_mfma_scale_f32_16x16x128_f8f6f4 v[142:145], v[26:33], v[206:213], 0, v234, v235 op_sel_hi:[0,0,0]
	v_mfma_scale_f32_16x16x128_f8f6f4 v[138:141], v[18:25], v[206:213], 0, v234, v235 op_sel_hi:[0,0,0]
	v_mfma_scale_f32_16x16x128_f8f6f4 v[134:137], v[26:33], v[216:223], 0, v234, v235 op_sel_hi:[0,0,0]
	v_mfma_scale_f32_16x16x128_f8f6f4 v[130:133], v[18:25], v[216:223], 0, v234, v235 op_sel_hi:[0,0,0]
	v_mfma_scale_f32_16x16x128_f8f6f4 v[126:129], v[26:33], v[224:231], 0, v234, v235 op_sel_hi:[0,0,0]
	v_mfma_scale_f32_16x16x128_f8f6f4 v[122:125], v[18:25], v[224:231], 0, v234, v235 op_sel_hi:[0,0,0]
	s_setprio 0
	s_setprio 1
	v_mfma_scale_f32_16x16x128_f8f6f4 v[118:121], v[10:17], v[198:205], 0, v234, v235 op_sel_hi:[0,0,0]
	v_mfma_scale_f32_16x16x128_f8f6f4 v[114:117], v[2:9], v[198:205], 0, v234, v235 op_sel_hi:[0,0,0]
	v_mfma_scale_f32_16x16x128_f8f6f4 v[110:113], v[10:17], v[206:213], 0, v234, v235 op_sel_hi:[0,0,0]
	v_mfma_scale_f32_16x16x128_f8f6f4 v[106:109], v[2:9], v[206:213], 0, v234, v235 op_sel_hi:[0,0,0]
	v_mfma_scale_f32_16x16x128_f8f6f4 v[102:105], v[10:17], v[216:223], 0, v234, v235 op_sel_hi:[0,0,0]
	v_mfma_scale_f32_16x16x128_f8f6f4 v[98:101], v[2:9], v[216:223], 0, v234, v235 op_sel_hi:[0,0,0]
	v_mfma_scale_f32_16x16x128_f8f6f4 v[94:97], v[10:17], v[224:231], 0, v234, v235 op_sel_hi:[0,0,0]
	v_mfma_scale_f32_16x16x128_f8f6f4 v[90:93], v[2:9], v[224:231], 0, v234, v235 op_sel_hi:[0,0,0]
	s_setprio 0
	s_barrier
	v_lshl_add_u64 v[170:171], s[4:5], 0, v[162:163]
	s_mov_b64 s[54:55], 0x100
	s_mov_b32 m0, s68
	v_lshl_add_u64 v[172:173], v[170:171], 0, s[54:55]
	ds_read_b128 v[198:201], v192 offset:16384
	ds_read_b128 v[202:205], v192 offset:17408
	ds_read_b128 v[206:209], v192 offset:18432
	ds_read_b128 v[210:213], v192 offset:19456
	ds_read_b128 v[216:219], v192 offset:20480
	ds_read_b128 v[220:223], v192 offset:21504
	ds_read_b128 v[224:227], v192 offset:22528
	ds_read_b128 v[228:231], v192 offset:23552
	global_load_lds_dwordx4 v[172:173], off
	v_lshl_add_u64 v[172:173], s[4:5], 0, v[164:165]
	v_lshl_add_u64 v[232:233], v[172:173], 0, s[54:55]
	s_add_u32 s54, s4, 0x20100
	s_mov_b32 m0, s60
	s_addc_u32 s55, s5, 0
	global_load_lds_dwordx4 v[232:233], off
	v_lshl_add_u64 v[232:233], s[54:55], 0, v[162:163]
	s_mov_b32 m0, s61
	v_lshlrev_b32_e32 v0, 10, v195
	global_load_lds_dwordx4 v[232:233], off
	v_lshl_add_u64 v[232:233], s[54:55], 0, v[164:165]
	s_mov_b32 m0, s62
	v_and_or_b32 v0, v0, s82, v174
	global_load_lds_dwordx4 v[232:233], off
	v_bfe_u32 v197, v195, 16, 16
	s_mov_b32 m0, s65
	v_lshl_add_u32 v197, v197, 10, v175
	global_load_lds_dwordx4 v0, s[34:35]
	s_mov_b32 m0, s63
	s_nop 0
	global_load_lds_dwordx4 v197, s[34:35]
	s_cmp_eq_u32 s23, 0
	s_cbranch_scc1 .Lrw_first_g1_1
	s_waitcnt vmcnt(12)
	s_branch .Lrw_done_g1_1

.Lrw_done_g1_1:
	s_waitcnt lgkmcnt(0)
	s_barrier
	s_setprio 1
	s_waitcnt lgkmcnt(0)
	v_mfma_scale_f32_16x16x128_f8f6f4 v[86:89], v[26:33], v[198:205], 0, v234, v235 op_sel_hi:[0,0,0]
	v_mfma_scale_f32_16x16x128_f8f6f4 v[82:85], v[18:25], v[198:205], 0, v234, v235 op_sel_hi:[0,0,0]
	v_mfma_scale_f32_16x16x128_f8f6f4 v[78:81], v[26:33], v[206:213], 0, v234, v235 op_sel_hi:[0,0,0]
	v_mfma_scale_f32_16x16x128_f8f6f4 v[74:77], v[18:25], v[206:213], 0, v234, v235 op_sel_hi:[0,0,0]
	v_mfma_scale_f32_16x16x128_f8f6f4 v[70:73], v[26:33], v[216:223], 0, v234, v235 op_sel_hi:[0,0,0]
	v_mfma_scale_f32_16x16x128_f8f6f4 v[66:69], v[18:25], v[216:223], 0, v234, v235 op_sel_hi:[0,0,0]
	v_mfma_scale_f32_16x16x128_f8f6f4 v[62:65], v[26:33], v[224:231], 0, v234, v235 op_sel_hi:[0,0,0]
	v_mfma_scale_f32_16x16x128_f8f6f4 v[58:61], v[18:25], v[224:231], 0, v234, v235 op_sel_hi:[0,0,0]
	s_setprio 0
	s_setprio 1
	v_mfma_scale_f32_16x16x128_f8f6f4 v[54:57], v[10:17], v[198:205], 0, v234, v235 op_sel_hi:[0,0,0]
	v_mfma_scale_f32_16x16x128_f8f6f4 v[50:53], v[2:9], v[198:205], 0, v234, v235 op_sel_hi:[0,0,0]
	v_mfma_scale_f32_16x16x128_f8f6f4 v[46:49], v[10:17], v[206:213], 0, v234, v235 op_sel_hi:[0,0,0]
	v_mfma_scale_f32_16x16x128_f8f6f4 v[42:45], v[2:9], v[206:213], 0, v234, v235 op_sel_hi:[0,0,0]
	v_mfma_scale_f32_16x16x128_f8f6f4 v[38:41], v[10:17], v[216:223], 0, v234, v235 op_sel_hi:[0,0,0]
	v_mfma_scale_f32_16x16x128_f8f6f4 v[34:37], v[2:9], v[216:223], 0, v234, v235 op_sel_hi:[0,0,0]
	v_mfma_scale_f32_16x16x128_f8f6f4 v[154:157], v[10:17], v[224:231], 0, v234, v235 op_sel_hi:[0,0,0]
	v_mfma_scale_f32_16x16x128_f8f6f4 v[158:161], v[2:9], v[224:231], 0, v234, v235 op_sel_hi:[0,0,0]
	s_setprio 0
	s_barrier
	ds_read_b128 v[18:21], v184
	ds_read_b128 v[22:25], v185
	ds_read_b128 v[26:29], v186
	ds_read_b128 v[30:33], v187
	ds_read_b128 v[2:5], v188
	ds_read_b128 v[6:9], v189
	ds_read_b128 v[10:13], v190
	ds_read_b128 v[14:17], v191
	s_mov_b32 m0, s10
	ds_read_b128 v[198:201], v192 offset:32768
	ds_read_b128 v[202:205], v192 offset:33792
	ds_read_b128 v[206:209], v192 offset:34816
	ds_read_b128 v[210:213], v192 offset:35840
	ds_read_b128 v[216:219], v192 offset:36864
	ds_read_b128 v[220:223], v192 offset:37888
	ds_read_b128 v[224:227], v192 offset:38912
	ds_read_b128 v[228:231], v192 offset:39936
	global_load_lds_dwordx4 v166, s[34:35]
	s_mov_b32 m0, s11
	s_nop 0
	global_load_lds_dwordx4 v168, s[34:35]
	s_waitcnt vmcnt(8)
	s_waitcnt lgkmcnt(0)
	s_barrier
	s_setprio 1
	s_waitcnt lgkmcnt(0)
	v_mfma_scale_f32_16x16x128_f8f6f4 v[150:153], v[18:25], v[198:205], v[150:153], v234, v235 op_sel_hi:[0,0,0]
	v_mfma_scale_f32_16x16x128_f8f6f4 v[146:149], v[26:33], v[198:205], v[146:149], v234, v235 op_sel_hi:[0,0,0]
	v_mfma_scale_f32_16x16x128_f8f6f4 v[142:145], v[18:25], v[206:213], v[142:145], v234, v235 op_sel_hi:[0,0,0]
	v_mfma_scale_f32_16x16x128_f8f6f4 v[138:141], v[26:33], v[206:213], v[138:141], v234, v235 op_sel_hi:[0,0,0]
	v_mfma_scale_f32_16x16x128_f8f6f4 v[134:137], v[18:25], v[216:223], v[134:137], v234, v235 op_sel_hi:[0,0,0]
	v_mfma_scale_f32_16x16x128_f8f6f4 v[130:133], v[26:33], v[216:223], v[130:133], v234, v235 op_sel_hi:[0,0,0]
	v_mfma_scale_f32_16x16x128_f8f6f4 v[126:129], v[18:25], v[224:231], v[126:129], v234, v235 op_sel_hi:[0,0,0]
	v_mfma_scale_f32_16x16x128_f8f6f4 v[122:125], v[26:33], v[224:231], v[122:125], v234, v235 op_sel_hi:[0,0,0]
	s_setprio 0
	s_setprio 1
	v_mfma_scale_f32_16x16x128_f8f6f4 v[118:121], v[2:9], v[198:205], v[118:121], v234, v235 op_sel_hi:[0,0,0]
	v_mfma_scale_f32_16x16x128_f8f6f4 v[114:117], v[10:17], v[198:205], v[114:117], v234, v235 op_sel_hi:[0,0,0]
	v_mfma_scale_f32_16x16x128_f8f6f4 v[110:113], v[2:9], v[206:213], v[110:113], v234, v235 op_sel_hi:[0,0,0]
	v_mfma_scale_f32_16x16x128_f8f6f4 v[106:109], v[10:17], v[206:213], v[106:109], v234, v235 op_sel_hi:[0,0,0]
	v_mfma_scale_f32_16x16x128_f8f6f4 v[102:105], v[2:9], v[216:223], v[102:105], v234, v235 op_sel_hi:[0,0,0]
	v_mfma_scale_f32_16x16x128_f8f6f4 v[98:101], v[10:17], v[216:223], v[98:101], v234, v235 op_sel_hi:[0,0,0]
	v_mfma_scale_f32_16x16x128_f8f6f4 v[94:97], v[2:9], v[224:231], v[94:97], v234, v235 op_sel_hi:[0,0,0]
	v_mfma_scale_f32_16x16x128_f8f6f4 v[90:93], v[10:17], v[224:231], v[90:93], v234, v235 op_sel_hi:[0,0,0]
	s_setprio 0
	s_barrier
	s_mov_b64 s[54:55], 0x180
	s_mov_b32 m0, s64
	v_lshl_add_u64 v[170:171], v[170:171], 0, s[54:55]
	ds_read_b128 v[198:201], v192 offset:49152
	ds_read_b128 v[202:205], v192 offset:50176
	ds_read_b128 v[206:209], v192 offset:51200
	ds_read_b128 v[210:213], v192 offset:52224
	ds_read_b128 v[216:219], v192 offset:53248
	ds_read_b128 v[220:223], v192 offset:54272
	ds_read_b128 v[224:227], v192 offset:55296
	ds_read_b128 v[228:231], v192 offset:56320
	global_load_lds_dwordx4 v[170:171], off
	v_lshl_add_u64 v[170:171], v[172:173], 0, s[54:55]
	s_add_u32 s54, s4, 0x20180
	s_mov_b32 m0, s81
	s_addc_u32 s55, s5, 0
	global_load_lds_dwordx4 v[170:171], off
	v_lshl_add_u64 v[170:171], s[54:55], 0, v[162:163]
	s_mov_b32 m0, s49
	s_nop 0
	global_load_lds_dwordx4 v[170:171], off
	v_lshl_add_u64 v[170:171], s[54:55], 0, v[164:165]
	s_mov_b32 m0, s30
	s_nop 0
	global_load_lds_dwordx4 v[170:171], off
	s_mov_b32 m0, s6
	s_nop 0
	global_load_lds_dwordx4 v0, s[36:37]
	s_mov_b32 m0, s7
	s_nop 0
	global_load_lds_dwordx4 v197, s[36:37]
	s_waitcnt vmcnt(8)
	s_waitcnt lgkmcnt(0)
	s_barrier
	s_setprio 1
	s_waitcnt lgkmcnt(0)
	v_mfma_scale_f32_16x16x128_f8f6f4 v[86:89], v[18:25], v[198:205], v[86:89], v234, v235 op_sel_hi:[0,0,0]
	v_mfma_scale_f32_16x16x128_f8f6f4 v[82:85], v[26:33], v[198:205], v[82:85], v234, v235 op_sel_hi:[0,0,0]
	v_mfma_scale_f32_16x16x128_f8f6f4 v[78:81], v[18:25], v[206:213], v[78:81], v234, v235 op_sel_hi:[0,0,0]
	v_mfma_scale_f32_16x16x128_f8f6f4 v[74:77], v[26:33], v[206:213], v[74:77], v234, v235 op_sel_hi:[0,0,0]
	v_mfma_scale_f32_16x16x128_f8f6f4 v[70:73], v[18:25], v[216:223], v[70:73], v234, v235 op_sel_hi:[0,0,0]
	v_mfma_scale_f32_16x16x128_f8f6f4 v[66:69], v[26:33], v[216:223], v[66:69], v234, v235 op_sel_hi:[0,0,0]
	v_mfma_scale_f32_16x16x128_f8f6f4 v[62:65], v[18:25], v[224:231], v[62:65], v234, v235 op_sel_hi:[0,0,0]
	v_mfma_scale_f32_16x16x128_f8f6f4 v[58:61], v[26:33], v[224:231], v[58:61], v234, v235 op_sel_hi:[0,0,0]
	s_setprio 0
	s_setprio 1
	v_mfma_scale_f32_16x16x128_f8f6f4 v[54:57], v[2:9], v[198:205], v[54:57], v234, v235 op_sel_hi:[0,0,0]
	v_mfma_scale_f32_16x16x128_f8f6f4 v[50:53], v[10:17], v[198:205], v[50:53], v234, v235 op_sel_hi:[0,0,0]
	v_mfma_scale_f32_16x16x128_f8f6f4 v[46:49], v[2:9], v[206:213], v[46:49], v234, v235 op_sel_hi:[0,0,0]
	v_mfma_scale_f32_16x16x128_f8f6f4 v[42:45], v[10:17], v[206:213], v[42:45], v234, v235 op_sel_hi:[0,0,0]
	v_mfma_scale_f32_16x16x128_f8f6f4 v[38:41], v[2:9], v[216:223], v[38:41], v234, v235 op_sel_hi:[0,0,0]
	v_mfma_scale_f32_16x16x128_f8f6f4 v[34:37], v[10:17], v[216:223], v[34:37], v234, v235 op_sel_hi:[0,0,0]
	v_mfma_scale_f32_16x16x128_f8f6f4 v[154:157], v[2:9], v[224:231], v[154:157], v234, v235 op_sel_hi:[0,0,0]
	v_mfma_scale_f32_16x16x128_f8f6f4 v[158:161], v[10:17], v[224:231], v[158:161], v234, v235 op_sel_hi:[0,0,0]
	s_setprio 0
	s_barrier
	s_add_u32 s43, s4, 0x200
	s_addc_u32 s45, s5, 0
	s_mov_b32 s74, 0
	s_mov_b64 s[54:55], s[36:37]
	s_branch .LBB0_2003

.LBB0_2088:
	ds_read_b128 v[18:21], v180
	ds_read_b128 v[22:25], v181
	ds_read_b128 v[26:29], v182
	ds_read_b128 v[30:33], v183
	ds_read_b128 v[2:5], v184
	ds_read_b128 v[6:9], v185
	ds_read_b128 v[10:13], v186
	ds_read_b128 v[14:17], v187
	s_ashr_i32 s13, s12, 31
	s_lshl_b64 s[38:39], s[12:13], 18
	s_add_u32 s38, s53, s38
	s_addc_u32 s39, s54, s39
	s_and_b64 s[46:47], s[48:49], exec
	s_cselect_b32 s13, s39, s43
	s_cselect_b32 s27, s38, s42
	s_add_u32 s46, s42, 0x20080
	s_addc_u32 s47, s43, 0
	s_add_i32 s29, s37, 0xc000
	v_lshl_add_u64 v[224:225], s[46:47], 0, v[162:163]
	s_mov_b32 m0, s29
	s_add_i32 s31, s37, 0xe000
	ds_read_b128 v[172:175], v196
	ds_read_b128 v[176:179], v196 offset:1024
	ds_read_b128 v[198:201], v196 offset:2048
	ds_read_b128 v[202:205], v196 offset:3072
	ds_read_b128 v[206:209], v196 offset:4096
	ds_read_b128 v[210:213], v196 offset:5120
	ds_read_b128 v[216:219], v196 offset:6144
	ds_read_b128 v[220:223], v196 offset:7168
	global_load_lds_dwordx4 v[224:225], off
	v_lshl_add_u64 v[224:225], s[46:47], 0, v[164:165]
	s_mov_b32 m0, s31
	s_nop 0
	global_load_lds_dwordx4 v[224:225], off
	s_cmp_eq_u32 s26, 0
	s_cbranch_scc1 .Lrw_first_g2_0
	s_waitcnt vmcnt(24)
	s_branch .Lrw_done_g2_0

.Lrw_done_g2_0:
	s_waitcnt lgkmcnt(0)
	s_barrier
	s_setprio 1
	s_waitcnt lgkmcnt(0)
	v_mfma_scale_f32_16x16x128_f8f6f4 v[158:161], v[18:25], v[172:179], 0, v234, v238 op_sel_hi:[0,0,0]
	v_mfma_scale_f32_16x16x128_f8f6f4 v[154:157], v[26:33], v[172:179], 0, v234, v238 op_sel_hi:[0,0,0]
	v_mfma_scale_f32_16x16x128_f8f6f4 v[150:153], v[18:25], v[198:205], 0, v234, v238 op_sel_hi:[0,0,0]
	v_mfma_scale_f32_16x16x128_f8f6f4 v[146:149], v[26:33], v[198:205], 0, v234, v238 op_sel_hi:[0,0,0]
	v_mfma_scale_f32_16x16x128_f8f6f4 v[142:145], v[18:25], v[206:213], 0, v234, v238 op_sel_hi:[0,0,0]
	v_mfma_scale_f32_16x16x128_f8f6f4 v[138:141], v[26:33], v[206:213], 0, v234, v238 op_sel_hi:[0,0,0]
	v_mfma_scale_f32_16x16x128_f8f6f4 v[134:137], v[18:25], v[216:223], 0, v234, v238 op_sel_hi:[0,0,0]
	v_mfma_scale_f32_16x16x128_f8f6f4 v[130:133], v[26:33], v[216:223], 0, v234, v238 op_sel_hi:[0,0,0]
	s_setprio 0
	s_setprio 1
	v_mfma_scale_f32_16x16x128_f8f6f4 v[126:129], v[2:9], v[172:179], 0, v234, v238 op_sel_hi:[0,0,0]
	v_mfma_scale_f32_16x16x128_f8f6f4 v[122:125], v[10:17], v[172:179], 0, v234, v238 op_sel_hi:[0,0,0]
	v_mfma_scale_f32_16x16x128_f8f6f4 v[118:121], v[2:9], v[198:205], 0, v234, v238 op_sel_hi:[0,0,0]
	v_mfma_scale_f32_16x16x128_f8f6f4 v[114:117], v[10:17], v[198:205], 0, v234, v238 op_sel_hi:[0,0,0]
	v_mfma_scale_f32_16x16x128_f8f6f4 v[110:113], v[2:9], v[206:213], 0, v234, v238 op_sel_hi:[0,0,0]
	v_mfma_scale_f32_16x16x128_f8f6f4 v[106:109], v[10:17], v[206:213], 0, v234, v238 op_sel_hi:[0,0,0]
	v_mfma_scale_f32_16x16x128_f8f6f4 v[102:105], v[2:9], v[216:223], 0, v234, v238 op_sel_hi:[0,0,0]
	v_mfma_scale_f32_16x16x128_f8f6f4 v[98:101], v[10:17], v[216:223], 0, v234, v238 op_sel_hi:[0,0,0]
	s_setprio 0
	s_barrier
	v_lshl_add_u64 v[172:173], s[44:45], 0, v[0:1]
	s_mov_b64 s[48:49], 0x100
	s_mov_b32 m0, s41
	v_lshl_add_u64 v[174:175], v[172:173], 0, s[48:49]
	ds_read_b128 v[198:201], v196 offset:16384
	ds_read_b128 v[202:205], v196 offset:17408
	ds_read_b128 v[206:209], v196 offset:18432
	ds_read_b128 v[210:213], v196 offset:19456
	ds_read_b128 v[216:219], v196 offset:20480
	ds_read_b128 v[220:223], v196 offset:21504
	ds_read_b128 v[224:227], v196 offset:22528
	ds_read_b128 v[228:231], v196 offset:23552
	global_load_lds_dwordx4 v[174:175], off
	v_lshl_add_u64 v[174:175], s[44:45], 0, v[166:167]
	s_add_u32 s46, s44, 0x20100
	v_lshl_add_u64 v[176:177], v[174:175], 0, s[48:49]
	s_mov_b32 m0, s57
	s_addc_u32 s47, s45, 0
	global_load_lds_dwordx4 v[176:177], off
	v_lshl_add_u64 v[176:177], s[46:47], 0, v[0:1]
	s_mov_b32 m0, s58
	s_nop 0
	global_load_lds_dwordx4 v[176:177], off
	v_lshl_add_u64 v[176:177], s[46:47], 0, v[166:167]
	s_mov_b32 m0, s59
	s_nop 0
	global_load_lds_dwordx4 v[176:177], off
	v_lshl_add_u64 v[176:177], s[42:43], 0, v[162:163]
	v_lshl_add_u64 v[178:179], v[176:177], 0, s[48:49]
	s_mov_b32 m0, s37
	s_nop 0
	global_load_lds_dwordx4 v[178:179], off
	v_lshl_add_u64 v[178:179], s[42:43], 0, v[164:165]
	v_lshl_add_u64 v[232:233], v[178:179], 0, s[48:49]
	s_mov_b32 m0, s60
	s_nop 0
	global_load_lds_dwordx4 v[232:233], off
	s_cmp_eq_u32 s26, 0
	s_cbranch_scc1 .Lrw_first_g2_1
	s_waitcnt vmcnt(24)
	s_branch .Lrw_done_g2_1

.Lrw_done_g2_1:
	s_waitcnt lgkmcnt(0)
	s_barrier
	s_setprio 1
	s_waitcnt lgkmcnt(0)
	v_mfma_scale_f32_16x16x128_f8f6f4 v[94:97], v[18:25], v[198:205], 0, v234, v238 op_sel_hi:[0,0,0]
	v_mfma_scale_f32_16x16x128_f8f6f4 v[90:93], v[26:33], v[198:205], 0, v234, v238 op_sel_hi:[0,0,0]
	v_mfma_scale_f32_16x16x128_f8f6f4 v[86:89], v[18:25], v[206:213], 0, v234, v238 op_sel_hi:[0,0,0]
	v_mfma_scale_f32_16x16x128_f8f6f4 v[82:85], v[26:33], v[206:213], 0, v234, v238 op_sel_hi:[0,0,0]
	v_mfma_scale_f32_16x16x128_f8f6f4 v[78:81], v[18:25], v[216:223], 0, v234, v238 op_sel_hi:[0,0,0]
	v_mfma_scale_f32_16x16x128_f8f6f4 v[74:77], v[26:33], v[216:223], 0, v234, v238 op_sel_hi:[0,0,0]
	v_mfma_scale_f32_16x16x128_f8f6f4 v[70:73], v[18:25], v[224:231], 0, v234, v238 op_sel_hi:[0,0,0]
	v_mfma_scale_f32_16x16x128_f8f6f4 v[66:69], v[26:33], v[224:231], 0, v234, v238 op_sel_hi:[0,0,0]
	s_setprio 0
	s_setprio 1
	v_mfma_scale_f32_16x16x128_f8f6f4 v[62:65], v[2:9], v[198:205], 0, v234, v238 op_sel_hi:[0,0,0]
	v_mfma_scale_f32_16x16x128_f8f6f4 v[58:61], v[10:17], v[198:205], 0, v234, v238 op_sel_hi:[0,0,0]
	v_mfma_scale_f32_16x16x128_f8f6f4 v[54:57], v[2:9], v[206:213], 0, v234, v238 op_sel_hi:[0,0,0]
	v_mfma_scale_f32_16x16x128_f8f6f4 v[50:53], v[10:17], v[206:213], 0, v234, v238 op_sel_hi:[0,0,0]
	v_mfma_scale_f32_16x16x128_f8f6f4 v[46:49], v[2:9], v[216:223], 0, v234, v238 op_sel_hi:[0,0,0]
	v_mfma_scale_f32_16x16x128_f8f6f4 v[42:45], v[10:17], v[216:223], 0, v234, v238 op_sel_hi:[0,0,0]
	v_mfma_scale_f32_16x16x128_f8f6f4 v[38:41], v[2:9], v[224:231], 0, v234, v238 op_sel_hi:[0,0,0]
	v_mfma_scale_f32_16x16x128_f8f6f4 v[34:37], v[10:17], v[224:231], 0, v234, v238 op_sel_hi:[0,0,0]
	s_setprio 0
	s_barrier
	ds_read_b128 v[18:21], v188
	ds_read_b128 v[22:25], v189
	ds_read_b128 v[26:29], v190
	ds_read_b128 v[30:33], v191
	ds_read_b128 v[2:5], v192
	ds_read_b128 v[6:9], v193
	ds_read_b128 v[10:13], v194
	ds_read_b128 v[14:17], v195
	s_add_u32 s46, s42, 0x20100
	s_addc_u32 s47, s43, 0
	s_mov_b32 m0, s61
	v_lshl_add_u64 v[232:233], s[46:47], 0, v[162:163]
	ds_read_b128 v[198:201], v196 offset:32768
	ds_read_b128 v[202:205], v196 offset:33792
	ds_read_b128 v[206:209], v196 offset:34816
	ds_read_b128 v[210:213], v196 offset:35840
	ds_read_b128 v[216:219], v196 offset:36864
	ds_read_b128 v[220:223], v196 offset:37888
	ds_read_b128 v[224:227], v196 offset:38912
	ds_read_b128 v[228:231], v196 offset:39936
	global_load_lds_dwordx4 v[232:233], off
	v_lshl_add_u64 v[232:233], s[46:47], 0, v[164:165]
	s_mov_b32 m0, s62
	s_nop 0
	global_load_lds_dwordx4 v[232:233], off
	s_waitcnt vmcnt(8)
	s_waitcnt lgkmcnt(0)
	s_barrier
	s_setprio 1
	s_waitcnt lgkmcnt(0)
	v_mfma_scale_f32_16x16x128_f8f6f4 v[158:161], v[18:25], v[198:205], v[158:161], v234, v238 op_sel_hi:[0,0,0]
	v_mfma_scale_f32_16x16x128_f8f6f4 v[154:157], v[26:33], v[198:205], v[154:157], v234, v238 op_sel_hi:[0,0,0]
	v_mfma_scale_f32_16x16x128_f8f6f4 v[150:153], v[18:25], v[206:213], v[150:153], v234, v238 op_sel_hi:[0,0,0]
	v_mfma_scale_f32_16x16x128_f8f6f4 v[146:149], v[26:33], v[206:213], v[146:149], v234, v238 op_sel_hi:[0,0,0]
	v_mfma_scale_f32_16x16x128_f8f6f4 v[142:145], v[18:25], v[216:223], v[142:145], v234, v238 op_sel_hi:[0,0,0]
	v_mfma_scale_f32_16x16x128_f8f6f4 v[138:141], v[26:33], v[216:223], v[138:141], v234, v238 op_sel_hi:[0,0,0]
	v_mfma_scale_f32_16x16x128_f8f6f4 v[134:137], v[18:25], v[224:231], v[134:137], v234, v238 op_sel_hi:[0,0,0]
	v_mfma_scale_f32_16x16x128_f8f6f4 v[130:133], v[26:33], v[224:231], v[130:133], v234, v238 op_sel_hi:[0,0,0]
	s_setprio 0
	s_setprio 1
	v_mfma_scale_f32_16x16x128_f8f6f4 v[126:129], v[2:9], v[198:205], v[126:129], v234, v238 op_sel_hi:[0,0,0]
	v_mfma_scale_f32_16x16x128_f8f6f4 v[122:125], v[10:17], v[198:205], v[122:125], v234, v238 op_sel_hi:[0,0,0]
	v_mfma_scale_f32_16x16x128_f8f6f4 v[118:121], v[2:9], v[206:213], v[118:121], v234, v238 op_sel_hi:[0,0,0]
	v_mfma_scale_f32_16x16x128_f8f6f4 v[114:117], v[10:17], v[206:213], v[114:117], v234, v238 op_sel_hi:[0,0,0]
	v_mfma_scale_f32_16x16x128_f8f6f4 v[110:113], v[2:9], v[216:223], v[110:113], v234, v238 op_sel_hi:[0,0,0]
	v_mfma_scale_f32_16x16x128_f8f6f4 v[106:109], v[10:17], v[216:223], v[106:109], v234, v238 op_sel_hi:[0,0,0]
	v_mfma_scale_f32_16x16x128_f8f6f4 v[102:105], v[2:9], v[224:231], v[102:105], v234, v238 op_sel_hi:[0,0,0]
	v_mfma_scale_f32_16x16x128_f8f6f4 v[98:101], v[10:17], v[224:231], v[98:101], v234, v238 op_sel_hi:[0,0,0]
	s_setprio 0
	s_barrier
	s_mov_b64 s[48:49], 0x180
	s_mov_b32 m0, s65
	v_lshl_add_u64 v[172:173], v[172:173], 0, s[48:49]
	s_add_u32 s46, s44, 0x20180
	ds_read_b128 v[198:201], v196 offset:49152
	ds_read_b128 v[202:205], v196 offset:50176
	ds_read_b128 v[206:209], v196 offset:51200
	ds_read_b128 v[210:213], v196 offset:52224
	ds_read_b128 v[216:219], v196 offset:53248
	ds_read_b128 v[220:223], v196 offset:54272
	ds_read_b128 v[224:227], v196 offset:55296
	ds_read_b128 v[228:231], v196 offset:56320
	global_load_lds_dwordx4 v[172:173], off
	v_lshl_add_u64 v[172:173], v[174:175], 0, s[48:49]
	s_mov_b32 m0, s68
	s_addc_u32 s47, s45, 0
	global_load_lds_dwordx4 v[172:173], off
	v_lshl_add_u64 v[172:173], s[46:47], 0, v[0:1]
	s_mov_b32 m0, s51
	s_nop 0
	global_load_lds_dwordx4 v[172:173], off
	v_lshl_add_u64 v[172:173], s[46:47], 0, v[166:167]
	s_mov_b32 m0, s4
	s_nop 0
	global_load_lds_dwordx4 v[172:173], off
	v_lshl_add_u64 v[172:173], v[176:177], 0, s[48:49]
	s_mov_b32 m0, s81
	s_nop 0
	global_load_lds_dwordx4 v[172:173], off
	v_lshl_add_u64 v[172:173], v[178:179], 0, s[48:49]
	s_mov_b32 m0, s50
	s_nop 0
	global_load_lds_dwordx4 v[172:173], off
	s_waitcnt vmcnt(8)
	s_waitcnt lgkmcnt(0)
	s_barrier
	s_setprio 1
	s_waitcnt lgkmcnt(0)
	v_mfma_scale_f32_16x16x128_f8f6f4 v[94:97], v[18:25], v[198:205], v[94:97], v234, v238 op_sel_hi:[0,0,0]
	v_mfma_scale_f32_16x16x128_f8f6f4 v[90:93], v[26:33], v[198:205], v[90:93], v234, v238 op_sel_hi:[0,0,0]
	v_mfma_scale_f32_16x16x128_f8f6f4 v[86:89], v[18:25], v[206:213], v[86:89], v234, v238 op_sel_hi:[0,0,0]
	v_mfma_scale_f32_16x16x128_f8f6f4 v[82:85], v[26:33], v[206:213], v[82:85], v234, v238 op_sel_hi:[0,0,0]
	v_mfma_scale_f32_16x16x128_f8f6f4 v[78:81], v[18:25], v[216:223], v[78:81], v234, v238 op_sel_hi:[0,0,0]
	v_mfma_scale_f32_16x16x128_f8f6f4 v[74:77], v[26:33], v[216:223], v[74:77], v234, v238 op_sel_hi:[0,0,0]
	v_mfma_scale_f32_16x16x128_f8f6f4 v[70:73], v[18:25], v[224:231], v[70:73], v234, v238 op_sel_hi:[0,0,0]
	v_mfma_scale_f32_16x16x128_f8f6f4 v[66:69], v[26:33], v[224:231], v[66:69], v234, v238 op_sel_hi:[0,0,0]
	s_setprio 0
	s_setprio 1
	v_mfma_scale_f32_16x16x128_f8f6f4 v[62:65], v[2:9], v[198:205], v[62:65], v234, v238 op_sel_hi:[0,0,0]
	v_mfma_scale_f32_16x16x128_f8f6f4 v[58:61], v[10:17], v[198:205], v[58:61], v234, v238 op_sel_hi:[0,0,0]
	v_mfma_scale_f32_16x16x128_f8f6f4 v[54:57], v[2:9], v[206:213], v[54:57], v234, v238 op_sel_hi:[0,0,0]
	v_mfma_scale_f32_16x16x128_f8f6f4 v[50:53], v[10:17], v[206:213], v[50:53], v234, v238 op_sel_hi:[0,0,0]
	v_mfma_scale_f32_16x16x128_f8f6f4 v[46:49], v[2:9], v[216:223], v[46:49], v234, v238 op_sel_hi:[0,0,0]
	v_mfma_scale_f32_16x16x128_f8f6f4 v[42:45], v[10:17], v[216:223], v[42:45], v234, v238 op_sel_hi:[0,0,0]
	v_mfma_scale_f32_16x16x128_f8f6f4 v[38:41], v[2:9], v[224:231], v[38:41], v234, v238 op_sel_hi:[0,0,0]
	v_mfma_scale_f32_16x16x128_f8f6f4 v[34:37], v[10:17], v[224:231], v[34:37], v234, v238 op_sel_hi:[0,0,0]
	s_setprio 0
	s_barrier
	s_add_u32 s42, s42, 0x20180
	s_addc_u32 s43, s43, 0
	s_add_u32 s48, s44, 0x200
	s_addc_u32 s49, s45, 0
	s_mov_b32 s74, 0
